# csr gather: nodes of a bucket ordered by number of 8-row passes so the 8 nodes of a wave finish together
# baseline (speedup 1.0000x reference)
.Lg4_start:
	v_lshl_or_b32 v60, v38, 4, v44
	v_lshlrev_b32_e32 v63, 2, v38
	v_sub_u32_e32 v57, v45, v63
	v_cmp_gt_u32_e32 vcc, 64, v60
	s_and_saveexec_b64 s[8:9], vcc
	s_cbranch_execz .Lg4_perm_done
	v_lshl_add_u32 v56, v60, 2, v57
	ds_read2_b32 v[58:59], v56 offset1:1
	s_waitcnt lgkmcnt(0)
	v_sub_u32_e32 v58, v59, v58
	v_add_u32_e32 v58, 7, v58
	v_lshrrev_b32_e32 v58, 3, v58
	v_min_u32_e32 v58, 7, v58
	v_mov_b32_e32 v59, 0
	s_mov_b32 s12, 0
	v_cmp_eq_u32_e64 s[46:47], 7, v58
	v_cmp_eq_u32_e64 s[48:49], 6, v58
	v_cmp_eq_u32_e64 s[50:51], 5, v58
	v_cmp_eq_u32_e64 s[52:53], 4, v58
	v_cmp_eq_u32_e64 s[54:55], 3, v58
	v_cmp_eq_u32_e64 s[56:57], 2, v58
	v_cmp_eq_u32_e64 s[58:59], 1, v58
	v_cmp_eq_u32_e64 s[2:3], 0, v58
	s_nop 1
	v_mbcnt_lo_u32_b32 v56, s46, 0
	v_mbcnt_hi_u32_b32 v56, s47, v56
	v_add_u32_e32 v56, s12, v56
	v_cndmask_b32_e64 v59, v59, v56, s[46:47]
	s_bcnt1_i32_b64 s13, s[46:47]
	s_add_i32 s12, s12, s13
	v_mbcnt_lo_u32_b32 v56, s48, 0
	v_mbcnt_hi_u32_b32 v56, s49, v56
	v_add_u32_e32 v56, s12, v56
	v_cndmask_b32_e64 v59, v59, v56, s[48:49]
	s_bcnt1_i32_b64 s13, s[48:49]
	s_add_i32 s12, s12, s13
	v_mbcnt_lo_u32_b32 v56, s50, 0
	v_mbcnt_hi_u32_b32 v56, s51, v56
	v_add_u32_e32 v56, s12, v56
	v_cndmask_b32_e64 v59, v59, v56, s[50:51]
	s_bcnt1_i32_b64 s13, s[50:51]
	s_add_i32 s12, s12, s13
	v_mbcnt_lo_u32_b32 v56, s52, 0
	v_mbcnt_hi_u32_b32 v56, s53, v56
	v_add_u32_e32 v56, s12, v56
	v_cndmask_b32_e64 v59, v59, v56, s[52:53]
	s_bcnt1_i32_b64 s13, s[52:53]
	s_add_i32 s12, s12, s13
	v_mbcnt_lo_u32_b32 v56, s54, 0
	v_mbcnt_hi_u32_b32 v56, s55, v56
	v_add_u32_e32 v56, s12, v56
	v_cndmask_b32_e64 v59, v59, v56, s[54:55]
	s_bcnt1_i32_b64 s13, s[54:55]
	s_add_i32 s12, s12, s13
	v_mbcnt_lo_u32_b32 v56, s56, 0
	v_mbcnt_hi_u32_b32 v56, s57, v56
	v_add_u32_e32 v56, s12, v56
	v_cndmask_b32_e64 v59, v59, v56, s[56:57]
	s_bcnt1_i32_b64 s13, s[56:57]
	s_add_i32 s12, s12, s13
	v_mbcnt_lo_u32_b32 v56, s58, 0
	v_mbcnt_hi_u32_b32 v56, s59, v56
	v_add_u32_e32 v56, s12, v56
	v_cndmask_b32_e64 v59, v59, v56, s[58:59]
	s_bcnt1_i32_b64 s13, s[58:59]
	s_add_i32 s12, s12, s13
	v_mbcnt_lo_u32_b32 v56, s2, 0
	v_mbcnt_hi_u32_b32 v56, s3, v56
	v_add_u32_e32 v56, s12, v56
	v_cndmask_b32_e64 v59, v59, v56, s[2:3]
	s_bcnt1_i32_b64 s13, s[2:3]
	s_add_i32 s12, s12, s13
	v_lshlrev_b32_e32 v56, 2, v59
	ds_write_b32 v56, v60
.Lg4_perm_done:
	s_or_b64 exec, exec, s[8:9]
	s_waitcnt lgkmcnt(0)
	s_barrier
	v_lshrrev_b32_e32 v62, 3, v60
	v_lshlrev_b32_e32 v56, 2, v62
	ds_read_b32 v62, v56
	v_and_b32_e32 v61, 7, v60
	v_lshlrev_b32_e32 v61, 4, v61
	v_sub_u32_e32 v60, v46, v38
	s_waitcnt lgkmcnt(0)
	v_lshl_add_u32 v58, v62, 2, v57
	v_add_u32_e32 v60, v60, v62
	v_cmp_gt_i32_e32 vcc, s14, v60
	s_and_saveexec_b64 s[8:9], vcc
	s_cbranch_execz .Lg4_end
	ds_read2_b32 v[56:57], v58 offset1:1
	v_mov_b32_e32 v0, 0
	v_mov_b32_e32 v1, 0
	v_mov_b32_e32 v2, 0
	v_mov_b32_e32 v3, 0
	v_mov_b32_e32 v4, 0
	v_mov_b32_e32 v5, 0
	v_mov_b32_e32 v6, 0
	v_mov_b32_e32 v7, 0
	v_mov_b32_e32 v8, 0
	v_mov_b32_e32 v9, 0
	v_mov_b32_e32 v10, 0
	v_mov_b32_e32 v11, 0
	v_mov_b32_e32 v12, 0
	v_mov_b32_e32 v13, 0
	v_mov_b32_e32 v14, 0
	v_mov_b32_e32 v15, 0
	v_mov_b32_e32 v63, 0xc378
	s_waitcnt lgkmcnt(0)
	v_sub_u32_e32 v59, v57, v56
	v_lshlrev_b32_e32 v58, 1, v56
	v_add_u32_e32 v58, 0x4000, v58
	v_cmp_lt_i32_e32 vcc, 0, v59
	s_and_saveexec_b64 s[10:11], vcc
	s_cbranch_execz .Lg4_loop_skip
	s_mov_b32 s15, 0
	s_mov_b64 s[2:3], 0
